# n41_outlds_pad0
# speedup vs baseline: 1.0224x; 1.0072x over previous
.LBB2_15:
	v_ashrrev_i32_e32 v163, 31, v162
	v_lshl_or_b32 v164, s30, 4, v132
	v_lshlrev_b64 v[130:131], 11, v[162:163]
	v_mov_b32_e32 v167, 0
	s_waitcnt lgkmcnt(0)
	s_mov_b64 s[50:51], s[0:1]
	v_lshl_add_u64 v[130:131], s[0:1], 0, v[130:131]
	v_lshlrev_b32_e32 v166, 4, v164
	v_lshl_add_u64 v[168:169], v[130:131], 0, v[166:167]
	global_load_dwordx2 v[170:171], v[168:169], off nt
	v_lshlrev_b32_e32 v142, 4, v140
	v_cmp_gt_u32_e64 s[2:3], 16, v140
	v_mov_b32_e32 v140, 0x10000
	v_lshlrev_b32_e32 v130, 8, v139
	v_lshlrev_b32_e32 v131, 4, v132
	v_lshlrev_b32_e32 v132, 3, v138
	v_lshl_or_b32 v177, v138, 14, v142
	v_lshl_or_b32 v139, v139, 11, v140
	v_lshlrev_b32_e32 v140, 10, v138
	v_xor_b32_e32 v138, 1, v138
	v_lshlrev_b32_e32 v141, 12, v1
	v_lshlrev_b32_e32 v138, 10, v138
	v_or3_b32 v179, v139, v138, v142
	v_add_u32_e32 v138, 0x1000, v141
	v_and_b32_e32 v180, 0x3000, v138
	v_add_u32_e32 v138, 0x1400, v141
	v_and_b32_e32 v181, 0x3400, v138
	v_add_u32_e32 v138, 0x1800, v141
	v_and_b32_e32 v182, 0x3800, v138
	v_add_u32_e32 v138, 0x1c00, v141
	v_and_b32_e32 v183, 0x3c00, v138
	s_movk_i32 s4, 0x2000
	v_mov_b32_e32 v138, 0x3000
	v_bitop3_b32 v184, v141, s4, v138 bitop3:0x6c
	v_add_u32_e32 v138, 0x2400, v141
	v_and_b32_e32 v185, 0x3400, v138
	v_add_u32_e32 v138, 0x2800, v141
	v_and_b32_e32 v186, 0x3800, v138
	v_add_u32_e32 v138, 0x2c00, v141
	v_and_b32_e32 v187, 0x3c00, v138
	v_add_u32_e32 v138, 0x3000, v141
	v_and_b32_e32 v188, 0x3000, v138
	v_add_u32_e32 v138, 0x3400, v141
	s_and_b32 s9, s7, 0xffff
	v_cmp_eq_u32_e32 vcc, s14, v133
	v_lshl_or_b32 v131, s16, 10, v131
	s_movk_i32 s0, 0x100
	v_lshlrev_b32_e32 v166, 12, v164
	v_and_b32_e32 v189, 0x3400, v138
	v_add_u32_e32 v138, 0x3800, v141
	s_cmp_lg_u64 vcc, exec
	v_lshl_add_u32 v131, s30, 15, v131
	v_cmp_gt_u32_e64 s[0:1], s0, v0
	v_lshl_add_u64 v[0:1], s[12:13], 0, v[166:167]
	v_and_b32_e32 v190, 0x3800, v138
	v_add_u32_e32 v138, 0x3c00, v141
	v_mov_b32_e32 v172, -1
	s_mov_b32 s11, 0x20000
	s_mov_b32 s10, 0x200400
	s_mov_b32 s8, s6
	s_cselect_b64 s[14:15], -1, 0
	v_or3_b32 v165, v131, v132, v130
	s_mov_b32 s17, 0
	v_cndmask_b32_e64 v133, 0, v137, s[0:1]
	v_cndmask_b32_e64 v132, 0, v136, s[0:1]
	v_cndmask_b32_e64 v131, 0, v135, s[0:1]
	v_cndmask_b32_e64 v130, 0, v134, s[0:1]
	v_cndmask_b32_e64 v137, v137, 0, s[0:1]
	v_cndmask_b32_e64 v136, v136, 0, s[0:1]
	v_cndmask_b32_e64 v135, v135, 0, s[0:1]
	v_cndmask_b32_e64 v134, v134, 0, s[0:1]
	v_or_b32_e32 v176, v141, v142
	v_lshl_add_u64 v[0:1], v[162:163], 2, v[0:1]
	v_or3_b32 v178, v139, v140, v142
	v_and_b32_e32 v191, 0x3c00, v138
	s_mov_b64 s[24:25], 0
	s_mov_b64 s[18:19], 0x400
	s_mov_b64 s[20:21], 0x800
	s_mov_b64 s[22:23], 0xc00
	s_mov_b32 s31, 0x40004000
	v_mov_b32_e32 v173, v172
	v_mov_b32_e32 v192, 0
	v_mov_b32_e32 v193, 0
	s_mov_b32 s33, 0
	v_add_u32_e32 v180, v180, v177
	v_add_u32_e32 v181, v181, v177
	v_add_u32_e32 v182, v182, v177
	v_add_u32_e32 v183, v183, v177
	v_add_u32_e32 v184, v184, v177
	v_add_u32_e32 v185, v185, v177
	v_add_u32_e32 v186, v186, v177
	v_add_u32_e32 v187, v187, v177
	v_add_u32_e32 v188, v188, v177
	v_add_u32_e32 v189, v189, v177
	v_add_u32_e32 v190, v190, v177
	v_add_u32_e32 v191, v191, v177
	v_mov_b32_e32 v166, v176
	v_lshlrev_b32_e32 v242, 12, v164
	v_lshl_add_u32 v242, v162, 2, v242
	v_lshlrev_b32_e32 v243, 11, v162
	v_lshl_add_u32 v243, v164, 4, v243
	v_readfirstlane_b32 s42, v176
	s_or_b32 s42, s42, 0x8000
	s_mov_b32 m0, s42
	s_lshl_b32 s36, s30, 15
	s_add_u32 s54, s6, s36
	s_addc_u32 s55, s7, 0
	s_mov_b64 s[40:41], s[54:55]
	s_mov_b32 s45, 0
	s_mov_b32 s58, 0x40000
	s_mov_b32 s46, 0x180000
	s_mov_b64 s[48:49], s[12:13]
	s_cmp_lg_u64 s[14:15], 0
	s_cselect_b32 s57, 1, 0
	s_cmp_lg_u64 s[0:1], 0
	s_cselect_b32 s59, 1, 0
	s_mov_b32 s47, 0
	s_mov_b32 s60, 0
	s_mov_b32 s44, 0
	s_add_u32 s52, s50, 8
	s_addc_u32 s53, s51, 0
	global_load_dwordx2 v[174:175], v243, s[52:53] nt
	s_add_u32 s52, s50, 0x200000
	s_addc_u32 s53, s51, 0
	s_waitcnt vmcnt(1)
	v_cvt_f32_f16_e32 v250, v170
	v_cvt_f32_f16_sdwa v251, v170 dst_sel:DWORD dst_unused:UNUSED_PAD src0_sel:WORD_1
	v_cvt_f32_f16_e32 v252, v171
	v_cvt_f32_f16_sdwa v253, v171 dst_sel:DWORD dst_unused:UNUSED_PAD src0_sel:WORD_1
	v_pk_add_f32 v[198:199], v[130:131], v[134:135]
	v_pk_add_f32 v[200:201], v[132:133], v[136:137]
	v_mov_b32_e32 v194, 0
	v_mov_b32_e32 v195, 0
	v_mov_b32_e32 v196, 0
	v_mov_b32_e32 v197, 0
	v_pk_add_f32 v[198:199], v[198:199], v[250:251]
	v_pk_add_f32 v[200:201], v[200:201], v[252:253]
	v_lshrrev_b32_e32 v249, 4, v176
	v_and_b32_e32 v248, 15, v249
	v_bfe_u32 v246, v249, 4, 2
	v_lshrrev_b32_e32 v247, 8, v249
	v_and_b32_e32 v245, 3, v247
	v_lshrrev_b32_e32 v244, 2, v247
	v_lshl_add_u32 v246, v244, 2, v246
	v_lshl_add_u32 v246, v245, 3, v246
	v_mul_u32_u24_e32 v244, 33, v248
	v_add_u32_e32 v244, v244, v246
	s_mov_b32 s36, 0x12000
	v_lshl_add_u32 v244, v244, 2, s36
	v_bfe_u32 v246, v249, 5, 1
	v_lshl_add_u32 v246, v247, 1, v246
	v_and_b32_e32 v245, 31, v249
	v_lshl_add_u32 v247, s30, 4, v246
	v_lshlrev_b32_e32 v247, 12, v247
	v_lshrrev_b32_e32 v248, 10, v165
	v_and_b32_e32 v248, 31, v248
	v_lshl_add_u32 v248, v248, 5, v245
	v_lshl_add_u32 v247, v248, 2, v247
	v_mul_u32_u24_e32 v246, 33, v246
	v_add_u32_e32 v246, v246, v245
	v_lshl_add_u32 v246, v246, 2, s36
	s_branch .Lrec_act
.Lrec_step:
	global_load_lds_dwordx4 v176, s[40:41] sc1
	global_load_lds_dwordx4 v176, s[40:41] offset:1024 sc1
	global_load_lds_dwordx4 v176, s[40:41] offset:2048 sc1
	global_load_lds_dwordx4 v176, s[40:41] offset:3072 sc1
	s_mov_b32 s45, s58
	s_mov_b32 s44, 0
	v_xor_b32_e32 v166, 0x8000, v166
	v_xor_b32_e32 v180, 0x8000, v180
	v_xor_b32_e32 v181, 0x8000, v181
	v_xor_b32_e32 v182, 0x8000, v182
	v_xor_b32_e32 v183, 0x8000, v183
	v_xor_b32_e32 v184, 0x8000, v184
	v_xor_b32_e32 v185, 0x8000, v185
	v_xor_b32_e32 v186, 0x8000, v186
	v_xor_b32_e32 v187, 0x8000, v187
	v_xor_b32_e32 v188, 0x8000, v188
	v_xor_b32_e32 v189, 0x8000, v189
	v_xor_b32_e32 v190, 0x8000, v190
	v_xor_b32_e32 v191, 0x8000, v191
	s_waitcnt vmcnt(4)
	v_cvt_f32_f16_e32 v250, v174
	v_cvt_f32_f16_sdwa v251, v174 dst_sel:DWORD dst_unused:UNUSED_PAD src0_sel:WORD_1
	v_cvt_f32_f16_e32 v252, v175
	v_cvt_f32_f16_sdwa v253, v175 dst_sel:DWORD dst_unused:UNUSED_PAD src0_sel:WORD_1
